# k_bin: loff pointer kernarg load hoisted to the binning branch entry
# baseline (speedup 1.0000x reference)
.LBB0_3:
	s_load_dwordx2 s[6:7], s[0:1], 0x0
	s_load_dwordx2 s[12:13], s[0:1], 0x8
	s_mul_i32 s4, s2, 0xc35
	s_mov_b32 s5, 0
	s_lshl_b64 s[8:9], s[4:5], 2
	v_mov_b32_e32 v3, 0
	s_waitcnt lgkmcnt(0)
	s_add_u32 s6, s6, s8
	s_addc_u32 s7, s7, s9
	s_add_u32 s8, s6, 0x30d400
	v_lshl_add_u64 v[4:5], s[6:7], 0, v[2:3]
	s_movk_i32 s3, 0x1000
	s_addc_u32 s9, s7, 0
	v_add_co_u32_e32 v4, vcc, s3, v4
	v_lshl_add_u64 v[6:7], s[8:9], 0, v[2:3]
	s_nop 0
	v_addc_co_u32_e32 v5, vcc, 0, v5, vcc
	v_or_b32_e32 v1, 0x1000, v2
	v_add_co_u32_e32 v6, vcc, s3, v6
	ds_write_b32 v2, v3 offset:12512
	s_waitcnt lgkmcnt(0)
	s_barrier
	global_load_dword v33, v2, s[8:9] offset:2048 nt
	global_load_dword v30, v2, s[8:9] offset:3072 nt
	v_addc_co_u32_e32 v7, vcc, 0, v7, vcc
	global_load_dword v28, v1, s[6:7] nt
	global_load_dword v29, v1, s[8:9] nt
	global_load_dword v20, v[4:5], off offset:1024 nt
	global_load_dword v21, v[6:7], off offset:1024 nt
	global_load_dword v16, v[4:5], off offset:2048 nt
	global_load_dword v17, v[6:7], off offset:2048 nt
	global_load_dword v14, v[6:7], off offset:3072 nt
	global_load_dword v15, v[4:5], off offset:3072 nt
	v_or_b32_e32 v1, 0x2000, v2
	v_or_b32_e32 v3, 0x2400, v2
	v_or_b32_e32 v4, 0x2800, v2
	v_or_b32_e32 v5, 0x2c00, v2
	global_load_dword v12, v1, s[6:7] nt
	global_load_dword v13, v1, s[8:9] nt
	global_load_dword v10, v3, s[6:7] nt
	global_load_dword v11, v3, s[8:9] nt
	global_load_dword v8, v4, s[6:7] nt
	global_load_dword v9, v4, s[8:9] nt
	global_load_dword v6, v5, s[6:7] nt
	global_load_dword v7, v5, s[8:9] nt
	v_or_b32_e32 v1, 0xc00, v0
	v_min_u32_e32 v1, 0xc34, v1
	v_lshlrev_b32_e32 v4, 2, v1
	global_load_dword v50, v2, s[6:7] nt
	global_load_dword v52, v2, s[8:9] nt
	global_load_dword v46, v2, s[6:7] offset:1024 nt
	global_load_dword v47, v2, s[8:9] offset:1024 nt
	global_load_dword v43, v2, s[6:7] offset:2048 nt
	global_load_dword v40, v2, s[6:7] offset:3072 nt
	global_load_dword v1, v4, s[6:7] nt
	global_load_dword v3, v4, s[8:9] nt
	s_waitcnt vmcnt(6)
	v_ashrrev_i32_e32 v4, 8, v52
	v_lshlrev_b32_e32 v55, 2, v4
	v_mov_b32_e32 v4, 1
	s_waitcnt vmcnt(4)
	v_ashrrev_i32_e32 v5, 8, v47
	ds_add_rtn_u32 v54, v55, v4 offset:12512
	v_lshlrev_b32_e32 v53, 2, v5
	v_ashrrev_i32_e32 v5, 8, v33
	ds_add_rtn_u32 v51, v53, v4 offset:12512
	v_lshlrev_b32_e32 v49, 2, v5
	v_ashrrev_i32_e32 v5, 8, v30
	ds_add_rtn_u32 v48, v49, v4 offset:12512
	v_lshlrev_b32_e32 v45, 2, v5
	v_ashrrev_i32_e32 v5, 8, v29
	ds_add_rtn_u32 v44, v45, v4 offset:12512
	v_lshlrev_b32_e32 v42, 2, v5
	v_ashrrev_i32_e32 v5, 8, v21
	ds_add_rtn_u32 v41, v42, v4 offset:12512
	v_lshlrev_b32_e32 v39, 2, v5
	v_ashrrev_i32_e32 v5, 8, v17
	ds_add_rtn_u32 v38, v39, v4 offset:12512
	v_lshlrev_b32_e32 v37, 2, v5
	v_ashrrev_i32_e32 v5, 8, v14
	ds_add_rtn_u32 v36, v37, v4 offset:12512
	v_lshlrev_b32_e32 v35, 2, v5
	v_ashrrev_i32_e32 v5, 8, v13
	ds_add_rtn_u32 v34, v35, v4 offset:12512
	v_lshlrev_b32_e32 v32, 2, v5
	ds_add_rtn_u32 v31, v32, v4 offset:12512
	s_movk_i32 s3, 0x335
	v_cmp_gt_u32_e32 vcc, s3, v0
	v_mov_b32_e32 v19, -1
	v_ashrrev_i32_e32 v27, 8, v11
	v_mov_b32_e32 v26, -1
	s_and_saveexec_b64 s[6:7], vcc
	v_lshlrev_b32_e32 v5, 2, v27
	ds_add_rtn_u32 v26, v5, v4 offset:12512
	s_or_b64 exec, exec, s[6:7]
	s_movk_i32 s3, 0x235
	v_cmp_gt_u32_e32 vcc, s3, v0
	v_ashrrev_i32_e32 v25, 8, v9
	s_and_saveexec_b64 s[6:7], vcc
	v_lshlrev_b32_e32 v4, 2, v25
	v_mov_b32_e32 v5, 1
	ds_add_rtn_u32 v19, v4, v5 offset:12512
	s_or_b64 exec, exec, s[6:7]
	s_movk_i32 s3, 0x135
	v_cmp_gt_u32_e32 vcc, s3, v0
	v_mov_b32_e32 v18, -1
	v_ashrrev_i32_e32 v23, 8, v7
	v_mov_b32_e32 v24, -1
	s_and_saveexec_b64 s[6:7], vcc
	v_lshlrev_b32_e32 v4, 2, v23
	v_mov_b32_e32 v5, 1
	ds_add_rtn_u32 v24, v4, v5 offset:12512
	s_or_b64 exec, exec, s[6:7]
	v_add_u32_e32 v4, 0x30e0, v2
	v_cmp_gt_u32_e32 vcc, 53, v0
	s_waitcnt vmcnt(0)
	v_ashrrev_i32_e32 v22, 8, v3
	s_and_saveexec_b64 s[6:7], vcc
	v_lshlrev_b32_e32 v5, 2, v22
	v_mov_b32_e32 v18, 1
	ds_add_rtn_u32 v18, v5, v18 offset:12512
	s_or_b64 exec, exec, s[6:7]
	v_mbcnt_lo_u32_b32 v5, -1, 0
	s_waitcnt lgkmcnt(0)
	s_barrier
	ds_read_b32 v4, v4
	v_mbcnt_hi_u32_b32 v5, -1, v5
	v_and_b32_e32 v56, 64, v5
	v_add_u32_e32 v57, -1, v5
	v_cmp_lt_i32_e32 vcc, v57, v56
	v_and_b32_e32 v58, 63, v0
	v_add_u32_e32 v59, -2, v5
	v_cndmask_b32_e32 v57, v57, v5, vcc
	v_lshlrev_b32_e32 v57, 2, v57
	s_waitcnt lgkmcnt(0)
	ds_bpermute_b32 v57, v57, v4
	v_cmp_ne_u32_e32 vcc, 0, v58
	s_waitcnt lgkmcnt(0)
	s_nop 0
	v_cndmask_b32_e32 v57, 0, v57, vcc
	v_cmp_lt_i32_e32 vcc, v59, v56
	v_add_u32_e32 v57, v57, v4
	s_nop 0
	v_cndmask_b32_e32 v59, v59, v5, vcc
	v_lshlrev_b32_e32 v59, 2, v59
	ds_bpermute_b32 v59, v59, v57
	v_cmp_lt_u32_e32 vcc, 1, v58
	s_waitcnt lgkmcnt(0)
	s_nop 0
	v_cndmask_b32_e32 v59, 0, v59, vcc
	v_add_u32_e32 v57, v59, v57
	v_add_u32_e32 v59, -4, v5
	v_cmp_lt_i32_e32 vcc, v59, v56
	s_nop 1
	v_cndmask_b32_e32 v59, v59, v5, vcc
	v_lshlrev_b32_e32 v59, 2, v59
	ds_bpermute_b32 v59, v59, v57
	v_cmp_lt_u32_e32 vcc, 3, v58
	s_waitcnt lgkmcnt(0)
	s_nop 0
	v_cndmask_b32_e32 v59, 0, v59, vcc
	v_add_u32_e32 v57, v59, v57
	v_add_u32_e32 v59, -8, v5
	v_cmp_lt_i32_e32 vcc, v59, v56
	s_nop 1
	v_cndmask_b32_e32 v59, v59, v5, vcc
	v_lshlrev_b32_e32 v59, 2, v59
	ds_bpermute_b32 v59, v59, v57
	v_cmp_lt_u32_e32 vcc, 7, v58
	s_waitcnt lgkmcnt(0)
	s_nop 0
	v_cndmask_b32_e32 v59, 0, v59, vcc
	v_add_u32_e32 v57, v59, v57
	v_add_u32_e32 v59, -16, v5
	v_cmp_lt_i32_e32 vcc, v59, v56
	s_nop 1
	v_cndmask_b32_e32 v59, v59, v5, vcc
	v_lshlrev_b32_e32 v59, 2, v59
	ds_bpermute_b32 v59, v59, v57
	v_cmp_lt_u32_e32 vcc, 15, v58
	s_waitcnt lgkmcnt(0)
	s_nop 0
	v_cndmask_b32_e32 v59, 0, v59, vcc
	v_add_u32_e32 v57, v59, v57
	v_subrev_u32_e32 v59, 32, v5
	v_cmp_lt_i32_e32 vcc, v59, v56
	s_nop 1
	v_cndmask_b32_e32 v5, v59, v5, vcc
	v_lshlrev_b32_e32 v5, 2, v5
	ds_bpermute_b32 v5, v5, v57
	v_cmp_lt_u32_e32 vcc, 31, v58
	s_waitcnt lgkmcnt(0)
	s_nop 0
	v_cndmask_b32_e32 v5, 0, v5, vcc
	v_add_u32_e32 v56, v5, v57
	v_cmp_eq_u32_e32 vcc, 63, v58
	s_and_saveexec_b64 s[6:7], vcc
	v_lshrrev_b32_e32 v5, 4, v0
	v_and_b32_e32 v5, 12, v5
	ds_write_b32 v5, v56 offset:14560
	s_or_b64 exec, exec, s[6:7]
	v_mov_b32_e32 v5, 0
	s_waitcnt lgkmcnt(0)
	s_barrier
	ds_read_b128 v[58:61], v5 offset:14560
	v_cmp_lt_u32_e32 vcc, 63, v0
	s_movk_i32 s3, 0x7f
	v_sub_u32_e32 v4, v56, v4
	s_waitcnt lgkmcnt(0)
	v_cndmask_b32_e32 v57, 0, v58, vcc
	v_cmp_lt_u32_e32 vcc, s3, v0
	s_movk_i32 s3, 0xbf
	s_nop 0
	v_cndmask_b32_e32 v58, 0, v59, vcc
	v_cmp_lt_u32_e32 vcc, s3, v0
	s_movk_i32 s3, 0xff
	s_nop 0
	v_cndmask_b32_e32 v59, 0, v60, vcc
	v_cmp_lt_u32_e32 vcc, s3, v0
	v_add3_u32 v57, v58, v57, v59
	s_movk_i32 s3, 0xc5
	v_cndmask_b32_e32 v58, 0, v61, vcc
	v_add3_u32 v56, v58, v57, v4
	v_cmp_gt_u32_e32 vcc, s3, v0
	ds_write_b32 v2, v56 offset:13536
	s_and_saveexec_b64 s[6:7], vcc
	s_cbranch_execz .LBB0_15
	v_lshl_or_b32 v4, v0, 8, s2
	s_waitcnt lgkmcnt(0)
	v_lshl_add_u64 v[4:5], v[4:5], 2, s[12:13]
	global_store_dword v[4:5], v56, off
